# P2 MMA-role causal masks computed once per item (role-guarded preheader), all four step copies use v_and
# baseline (speedup 1.0000x reference)
; DI int crow(int reg, int h) { return (reg & 3) + 8 * (reg >> 2) + 4 * h; }
; DI void h_chain(f32x16& S, f32x16& O, HPacks& K, const HOpsK& P, const bf16x8 (&vt)[2], const u32x4 (&vv)[2], int rq, int hh) {
;     ...
;     for (int i = 0; i < 16; ++i) X[i] = (crow(i, hh) <= rq) ? X[i] : 0.f;
; DI void p2_hgrn_roles(Frame& F, ArgsP A) {
;     ...
;     for (int item = F.vcu; item < 256; item += F.G) {
;         const int bh = item >> 1, vhalf = item & 1, b = bh >> 4, h = bh & 15;
;         const size_t rb = (size_t)b * SEQ * D;
;         unsigned CR[72];
;         f32x16 S0, S1;
; #pragma unroll
;         for (int i = 0; i < 72; ++i) CR[i] = 0u;
; #pragma unroll
;         for (int i = 0; i < 16; ++i) { S0[i] = 0.f; S1[i] = 0.f; }
.LBB0_411:
	s_and_b64 vcc, exec, s[42:43]
	s_cbranch_vccz .Lp2_nomask
	v_and_b32_e32 v243, 31, v0
	v_bfe_u32 v244, v0, 5, 1
	v_lshlrev_b32_e32 v244, 2, v244
	v_or_b32_e32 v245, 8, v244
	v_cmp_gt_i32_e64 s[100:101], v245, v243
	s_nop 1
	v_cndmask_b32_e64 v176, -1, 0, s[100:101]
	v_or_b32_e32 v245, 9, v244
	v_cmp_gt_i32_e64 s[100:101], v245, v243
	s_nop 1
	v_cndmask_b32_e64 v177, -1, 0, s[100:101]
	v_or_b32_e32 v245, 10, v244
	v_cmp_gt_i32_e64 s[100:101], v245, v243
	s_nop 1
	v_cndmask_b32_e64 v178, -1, 0, s[100:101]
	v_or_b32_e32 v245, 11, v244
	v_cmp_gt_i32_e64 s[100:101], v245, v243
	s_nop 1
	v_cndmask_b32_e64 v179, -1, 0, s[100:101]
	v_or_b32_e32 v245, 16, v244
	v_cmp_gt_i32_e64 s[100:101], v245, v243
	s_nop 1
	v_cndmask_b32_e64 v180, -1, 0, s[100:101]
	v_or_b32_e32 v245, 17, v244
	v_cmp_gt_i32_e64 s[100:101], v245, v243
	s_nop 1
	v_cndmask_b32_e64 v181, -1, 0, s[100:101]
	v_or_b32_e32 v245, 18, v244
	v_cmp_gt_i32_e64 s[100:101], v245, v243
	s_nop 1
	v_cndmask_b32_e64 v182, -1, 0, s[100:101]
	v_or_b32_e32 v245, 19, v244
	v_cmp_gt_i32_e64 s[100:101], v245, v243
	s_nop 1
	v_cndmask_b32_e64 v183, -1, 0, s[100:101]
	v_or_b32_e32 v245, 24, v244
	v_cmp_gt_i32_e64 s[100:101], v245, v243
	s_nop 1
	v_cndmask_b32_e64 v184, -1, 0, s[100:101]
	v_or_b32_e32 v245, 25, v244
	v_cmp_gt_i32_e64 s[100:101], v245, v243
	s_nop 1
	v_cndmask_b32_e64 v185, -1, 0, s[100:101]
	v_or_b32_e32 v245, 26, v244
	v_cmp_gt_i32_e64 s[100:101], v245, v243
	s_nop 1
	v_cndmask_b32_e64 v186, -1, 0, s[100:101]
	v_or_b32_e32 v245, 27, v244
	v_cmp_gt_i32_e64 s[100:101], v245, v243
	s_nop 1
	v_cndmask_b32_e64 v187, -1, 0, s[100:101]
	v_cmp_lt_i32_e64 s[100:101], v244, v243
	s_nop 1
	v_cndmask_b32_e64 v188, 0, -1, s[100:101]
	v_or_b32_e32 v245, 2, v244
	v_cmp_gt_i32_e64 s[100:101], v245, v243
	s_nop 1
	v_cndmask_b32_e64 v189, -1, 0, s[100:101]
	v_or_b32_e32 v245, 3, v244
	v_cmp_gt_i32_e64 s[100:101], v245, v243
	s_nop 1
	v_cndmask_b32_e64 v190, -1, 0, s[100:101]
	v_cmp_gt_i32_e64 s[100:101], v244, v243
	s_nop 1
	v_cndmask_b32_e64 v191, -1, 0, s[100:101]

; #define LAS __attribute__((address_space(3)))
; #define LDS_WAIT() asm volatile("s_waitcnt lgkmcnt(0)" ::: "memory")
; DI int crow(int reg, int h) { return (reg & 3) + 8 * (reg >> 2) + 4 * h; }
; DI void h_mma2(f32x16& S0, f32x16& S1, LAS unsigned char* buf, LAS unsigned char* red, int kbp, int vb, int r32, int hh) {
;     int rq = r32; asm volatile("" : "+v"(rq));
;     bf16x8 vt[2]; u32x4 vv[2];
; #pragma unroll
;     for (int st = 0; st < 2; ++st) {
;         vt[st] = *(const LAS bf16x8*)(buf + H_VT + (vb * 32 + r32) * 80 + (16 * st + 8 * hh) * 2);
;         const LAS unsigned char* vp = buf + H_VT + (vb * 32 + r32) * 80 + (16 * st + 4 * hh) * 2;
;         const u32x2 v0 = *(const LAS u32x2*)vp, v1 = *(const LAS u32x2*)(vp + 16);
;         vv[st].x = v0.x; vv[st].y = v0.y; vv[st].z = v1.x; vv[st].w = v1.y;
;     }
;     f32x16 Osum;
; #pragma unroll
;     for (int kk = 0; kk < 2; ++kk) {
;         HOpsK P; h_opsk_load(P, buf, 2 * kbp + kk, r32, hh);
;         f32x16& S = (kk == 0) ? S0 : S1; f32x16 O;
;         LDS_WAIT(); __builtin_amdgcn_sched_barrier(0);
;         HPacks K;
;         h_chain(S, O, K, P, vt, vv, rq, hh);
;         { float s_ = S[15] + O[15]; asm volatile("v_mov_b32 %0, %0" : "+v"(s_)); asm volatile("" :: "v"(s_)); }
;         asm volatile("" :: "v"(P.ka[0]), "v"(P.ka[1]), "v"(P.qb[0]), "v"(P.qb[1]), "v"(P.ku[0]), "v"(P.ku[1]), "v"(P.qq[0]), "v"(P.qq[1]));
;         asm volatile("" :: "v"(K.sp0), "v"(K.sp1), "v"(K.xp0), "v"(K.xp1));
;         __builtin_amdgcn_sched_barrier(0);
; #pragma unroll
;         for (int i = 0; i < 16; ++i) Osum[i] = (kk == 0) ? O[i] : Osum[i] + O[i];
;         __builtin_amdgcn_sched_barrier(0);
;     }
;     asm volatile("" :: "v"(vt[0]), "v"(vt[1]), "v"(vv[0]), "v"(vv[1]));
; #pragma unroll
;     for (int i = 0; i < 16; ++i) *(LAS float*)(red + ((kbp * 32 + crow(i, hh)) * 64 + vb * 32 + r32) * 4) = Osum[i];
.LBB0_413:
	s_and_b32 s4, s39, 1
	v_mov_b32_e32 v2, v0
	s_mul_i32 s5, s4, 0xb400
	s_add_i32 s62, s5, 0
	v_and_b32_e32 v193, 31, v2
	v_bfe_u32 v2, v2, 5, 1
	v_or_b32_e32 v5, s3, v193
	v_mov_b32_e32 v6, s62
	s_lshl_b32 s4, s4, 14
	v_lshlrev_b32_e32 v4, 8, v2
	v_mad_u32_u24 v5, v5, s86, v6
	v_lshlrev_b32_e32 v226, 4, v2
	v_lshlrev_b32_e32 v218, 3, v2
	s_add_i32 s4, s4, 0
	v_or3_b32 v4, v4, s73, v193
	v_add_u32_e32 v7, v5, v226
	v_add_u32_e32 v5, v5, v218
	v_lshl_add_u32 v242, v4, 2, s4
	v_mov_b32_e32 v4, v193
	v_add_u32_e32 v5, 0x8800, v5
	v_lshlrev_b32_e32 v2, 2, v2
	ds_read2_b64 v[100:103], v5 offset0:192 offset1:194
	ds_read2_b64 v[104:107], v5 offset0:196 offset1:198
	ds_read_b128 v[108:111], v7 offset:36352
	ds_read_b128 v[112:115], v7 offset:36384
	v_mad_u32_u24 v219, v193, s87, v6
	v_or_b32_e32 v4, s63, v218
	v_add_u32_e32 v222, v219, v218
	v_lshl_add_u32 v4, v4, 1, v219
	ds_read_b128 v[84:87], v4 offset:17408
	ds_read_b128 v[88:91], v4 offset:8704
	v_add_u32_e32 v4, s64, v222
	v_add_u32_e32 v4, 0x2000, v4
	v_add_u32_e32 v220, s62, v226
	v_or_b32_e32 v2, s63, v193
	ds_read2_b64 v[92:95], v4 offset0:64 offset1:66
	v_or_b32_e32 v4, s65, v218
	v_mad_u32_u24 v2, v2, s86, v220
	v_lshl_add_u32 v4, v4, 1, v219
	ds_read_b128 v[96:99], v4 offset:17408
	ds_read_b128 v[194:197], v4 offset:8704
	ds_read_b128 v[198:201], v2 offset:26112
	ds_read_b128 v[202:205], v2 offset:26144
	v_add_u32_e32 v2, s66, v222
	v_add_u32_e32 v2, 0x2000, v2
	ds_read2_b64 v[206:209], v2 offset0:64 offset1:66
	v_or_b32_e32 v2, s67, v226
	v_add_u32_e32 v2, s62, v2
	ds_read_b128 v[4:7], v2 offset:41472
	ds_read_b128 v[8:11], v2 offset:41504
	ds_read_b128 v[12:15], v2 offset:44032
	ds_read_b128 v[16:19], v2 offset:44064
	ds_read_b128 v[20:23], v2 offset:41536
	ds_read_b128 v[24:27], v2 offset:41568
	ds_read_b128 v[28:31], v2 offset:44096
	ds_read_b128 v[32:35], v2 offset:44128
	s_waitcnt lgkmcnt(0)
	s_waitcnt lgkmcnt(1)
	v_pk_mul_f32 v[28:29], v[60:61], v[28:29]
	v_pk_mul_f32 v[30:31], v[62:63], v[30:31]
	s_waitcnt lgkmcnt(0)
	v_pk_mul_f32 v[32:33], v[64:65], v[32:33]
	v_pk_mul_f32 v[34:35], v[66:67], v[34:35]
	v_pk_mul_f32 v[12:13], v[52:53], v[12:13]
	v_pk_mul_f32 v[14:15], v[54:55], v[14:15]
	v_pk_mul_f32 v[16:17], v[56:57], v[16:17]
	v_pk_mul_f32 v[18:19], v[58:59], v[18:19]
	v_cvt_pk_bf16_f32 v214, v28, v29
	v_cvt_pk_bf16_f32 v215, v30, v31
	v_cvt_pk_bf16_f32 v216, v32, v33
	v_cvt_pk_bf16_f32 v217, v34, v35
	v_pk_mul_f32 v[34:35], v[66:67], v[26:27]
	v_pk_mul_f32 v[30:31], v[62:63], v[22:23]
	v_pk_mul_f32 v[26:27], v[58:59], v[10:11]
	v_pk_mul_f32 v[22:23], v[54:55], v[6:7]
	v_pk_mul_f32 v[32:33], v[64:65], v[24:25]
	v_pk_mul_f32 v[28:29], v[60:61], v[20:21]
	v_pk_mul_f32 v[24:25], v[56:57], v[8:9]
	v_pk_mul_f32 v[20:21], v[52:53], v[4:5]
	v_cvt_pk_bf16_f32 v210, v12, v13
	v_cvt_pk_bf16_f32 v211, v14, v15
	v_cvt_pk_bf16_f32 v212, v16, v17
	v_cvt_pk_bf16_f32 v213, v18, v19
	v_mfma_f32_32x32x16_bf16 v[4:19], v[84:87], v[88:91], 0
	v_mfma_f32_32x32x16_bf16 v[4:19], v[96:99], v[194:197], v[4:19]
	s_nop 11
	v_and_b32_e32 v2, v191, v4
	v_and_b32_e32 v4, v188, v5
	v_and_b32_e32 v5, v189, v6
	v_and_b32_e32 v6, v190, v7
	v_and_b32_e32 v7, v176, v8
	v_and_b32_e32 v8, v177, v9
	v_and_b32_e32 v9, v178, v10
	v_and_b32_e32 v10, v179, v11
	v_and_b32_e32 v11, v180, v12
	v_and_b32_e32 v12, v181, v13
	v_and_b32_e32 v13, v182, v14
	v_and_b32_e32 v14, v183, v15
	v_and_b32_e32 v15, v184, v16
	v_and_b32_e32 v16, v185, v17
	v_and_b32_e32 v17, v186, v18
	v_and_b32_e32 v18, v187, v19
	v_cvt_pk_bf16_f32 v4, v2, v4
	v_cvt_pk_bf16_f32 v5, v5, v6
	v_cvt_pk_bf16_f32 v6, v7, v8
	v_cvt_pk_bf16_f32 v7, v9, v10
	v_cvt_pk_bf16_f32 v8, v11, v12
	v_cvt_pk_bf16_f32 v9, v13, v14
	v_cvt_pk_bf16_f32 v10, v15, v16
	v_cvt_pk_bf16_f32 v11, v17, v18
	v_mfma_f32_32x32x16_bf16 v[68:83], v[4:7], v[100:103], 0
	v_mfma_f32_32x32x16_bf16 v[68:83], v[92:95], v[210:213], v[68:83]
	v_mfma_f32_32x32x16_bf16 v[20:35], v[198:201], v[108:111], v[20:35]
	v_mfma_f32_32x32x16_bf16 v[68:83], v[8:11], v[104:107], v[68:83]
	v_mfma_f32_32x32x16_bf16 v[20:35], v[202:205], v[112:115], v[20:35]
	v_mfma_f32_32x32x16_bf16 v[68:83], v[206:209], v[214:217], v[68:83]
	s_nop 11
	v_add_f32_e32 v2, v83, v35
	v_mov_b32 v2, v2
	s_nop 0
	v_or_b32_e32 v4, s68, v218
	v_lshl_add_u32 v4, v4, 1, v219
	ds_read_b128 v[194:197], v4 offset:17408
	ds_read_b128 v[198:201], v4 offset:8704
	v_add_u32_e32 v4, s69, v222
	v_add_u32_e32 v4, 0x2000, v4
	v_or_b32_e32 v2, s68, v193
	ds_read2_b64 v[202:205], v4 offset0:64 offset1:66
	v_or_b32_e32 v4, s70, v218
	v_mad_u32_u24 v2, v2, s86, v220
	v_lshl_add_u32 v4, v4, 1, v219
	ds_read_b128 v[206:209], v4 offset:17408
	ds_read_b128 v[210:213], v4 offset:8704
	ds_read_b128 v[214:217], v2 offset:26112
	ds_read_b128 v[218:221], v2 offset:26144
	v_add_u32_e32 v2, s71, v222
	v_add_u32_e32 v2, 0x2000, v2
	ds_read2_b64 v[222:225], v2 offset0:64 offset1:66
	v_or_b32_e32 v2, s72, v226
	v_add_u32_e32 v2, s62, v2
	ds_read_b128 v[4:7], v2 offset:41472
	ds_read_b128 v[8:11], v2 offset:41504
	ds_read_b128 v[12:15], v2 offset:44032
	ds_read_b128 v[16:19], v2 offset:44064
	ds_read_b128 v[84:87], v2 offset:41536
	ds_read_b128 v[88:91], v2 offset:41568
	ds_read_b128 v[92:95], v2 offset:44096
	ds_read_b128 v[96:99], v2 offset:44128
	s_waitcnt lgkmcnt(0)
; DI void h_chain(f32x16& S, f32x16& O, HPacks& K, const HOpsK& P, const bf16x8 (&vt)[2], const u32x4 (&vv)[2], int rq, int hh) {
;     f32x16 X;
;     { f32x16 Se;
; #pragma unroll
;       for (int g = 0; g < 4; ++g) {
; #pragma unroll
;           for (int e = 0; e < 4; ++e) Se[4 * g + e] = S[4 * g + e] * P.ebm[g][e]; }
;       K.sp0 = pack_step(Se, 0); K.sp1 = pack_step(Se, 1); }
; #pragma unroll
;     for (int g = 0; g < 4; ++g) {
; #pragma unroll
;         for (int e = 0; e < 4; ++e) S[4 * g + e] *= P.dec[g][e]; }
; #pragma unroll
;     for (int i = 0; i < 16; ++i) { X[i] = 0.f; O[i] = 0.f; }
;     __builtin_amdgcn_sched_barrier(0);
; #pragma unroll
;     for (int st = 0; st < 2; ++st) X = MFMA32(P.ka[st], P.qb[st], X);
; #pragma unroll
;     for (int i = 0; i < 16; ++i) X[i] = (crow(i, hh) <= rq) ? X[i] : 0.f;
;     K.xp0 = pack_step(X, 0); K.xp1 = pack_step(X, 1);
;     __builtin_amdgcn_sched_barrier(0);
;     O = MFMA32(K.xp0, __builtin_bit_cast(bf16x8, vv[0]), O);
;     O = MFMA32(__builtin_bit_cast(bf16x8, P.qq[0]), K.sp0, O);
;     O = MFMA32(K.xp1, __builtin_bit_cast(bf16x8, vv[1]), O);
;     O = MFMA32(__builtin_bit_cast(bf16x8, P.qq[1]), K.sp1, O);
; #pragma unroll
;     for (int st = 0; st < 2; ++st) S = MFMA32(P.ku[st], vt[st], S);
;     __builtin_amdgcn_sched_barrier(0);
; }
; DI void h_mma2(f32x16& S0, f32x16& S1, LAS unsigned char* buf, LAS unsigned char* red, int kbp, int vb, int r32, int hh) {
;     int rq = r32; asm volatile("" : "+v"(rq));
;     bf16x8 vt[2]; u32x4 vv[2];
; #pragma unroll
;     for (int st = 0; st < 2; ++st) {
;         vt[st] = *(const LAS bf16x8*)(buf + H_VT + (vb * 32 + r32) * 80 + (16 * st + 8 * hh) * 2);
;         const LAS unsigned char* vp = buf + H_VT + (vb * 32 + r32) * 80 + (16 * st + 4 * hh) * 2;
;         const u32x2 v0 = *(const LAS u32x2*)vp, v1 = *(const LAS u32x2*)(vp + 16);
;         vv[st].x = v0.x; vv[st].y = v0.y; vv[st].z = v1.x; vv[st].w = v1.y;
;     }
;     f32x16 Osum;
; #pragma unroll
;     for (int kk = 0; kk < 2; ++kk) {
;         HOpsK P; h_opsk_load(P, buf, 2 * kbp + kk, r32, hh);
;         f32x16& S = (kk == 0) ? S0 : S1; f32x16 O;
;         LDS_WAIT(); __builtin_amdgcn_sched_barrier(0);
;         HPacks K;
;         h_chain(S, O, K, P, vt, vv, rq, hh);
;         { float s_ = S[15] + O[15]; asm volatile("v_mov_b32 %0, %0" : "+v"(s_)); asm volatile("" :: "v"(s_)); }
	s_waitcnt lgkmcnt(5)
	v_pk_mul_f32 v[12:13], v[36:37], v[12:13]
	v_pk_mul_f32 v[14:15], v[38:39], v[14:15]
	s_waitcnt lgkmcnt(4)
	v_pk_mul_f32 v[16:17], v[40:41], v[16:17]
	v_pk_mul_f32 v[18:19], v[42:43], v[18:19]
	s_waitcnt lgkmcnt(1)
	v_pk_mul_f32 v[92:93], v[44:45], v[92:93]
	v_pk_mul_f32 v[94:95], v[46:47], v[94:95]
	s_waitcnt lgkmcnt(0)
	v_pk_mul_f32 v[96:97], v[48:49], v[96:97]
	v_pk_mul_f32 v[98:99], v[50:51], v[98:99]
	v_cvt_pk_bf16_f32 v226, v12, v13
	v_cvt_pk_bf16_f32 v227, v14, v15
	v_cvt_pk_bf16_f32 v228, v16, v17
	v_cvt_pk_bf16_f32 v229, v18, v19
	v_pk_mul_f32 v[18:19], v[50:51], v[90:91]
	v_pk_mul_f32 v[14:15], v[46:47], v[86:87]
	v_pk_mul_f32 v[10:11], v[42:43], v[10:11]
	v_pk_mul_f32 v[6:7], v[38:39], v[6:7]
	v_pk_mul_f32 v[16:17], v[48:49], v[88:89]
	v_pk_mul_f32 v[12:13], v[44:45], v[84:85]
	v_pk_mul_f32 v[8:9], v[40:41], v[8:9]
	v_pk_mul_f32 v[4:5], v[36:37], v[4:5]
	v_cvt_pk_bf16_f32 v230, v92, v93
	v_cvt_pk_bf16_f32 v231, v94, v95
	v_cvt_pk_bf16_f32 v232, v96, v97
	v_cvt_pk_bf16_f32 v233, v98, v99
	v_mfma_f32_32x32x16_bf16 v[84:99], v[194:197], v[198:201], 0
	v_mfma_f32_32x32x16_bf16 v[84:99], v[206:209], v[210:213], v[84:99]
	s_nop 11
	v_and_b32_e32 v2, v191, v84
	v_and_b32_e32 v84, v188, v85
	v_and_b32_e32 v85, v189, v86
	v_and_b32_e32 v86, v190, v87
	v_and_b32_e32 v87, v176, v88
	v_and_b32_e32 v88, v177, v89
	v_and_b32_e32 v89, v178, v90
	v_and_b32_e32 v90, v179, v91
	v_and_b32_e32 v91, v180, v92
	v_and_b32_e32 v92, v181, v93
	v_and_b32_e32 v93, v182, v94
	v_and_b32_e32 v94, v183, v95
	v_and_b32_e32 v95, v184, v96
	v_and_b32_e32 v96, v185, v97
	v_and_b32_e32 v97, v186, v98
	v_and_b32_e32 v98, v187, v99
	v_cvt_pk_bf16_f32 v234, v2, v84
	v_cvt_pk_bf16_f32 v235, v85, v86
	v_cvt_pk_bf16_f32 v236, v87, v88
	v_cvt_pk_bf16_f32 v237, v89, v90
	v_cvt_pk_bf16_f32 v238, v91, v92
	v_cvt_pk_bf16_f32 v239, v93, v94
	v_cvt_pk_bf16_f32 v240, v95, v96
	v_cvt_pk_bf16_f32 v241, v97, v98
	v_mfma_f32_32x32x16_bf16 v[84:99], v[234:237], v[100:103], 0
	v_mfma_f32_32x32x16_bf16 v[84:99], v[202:205], v[226:229], v[84:99]
	v_mfma_f32_32x32x16_bf16 v[4:19], v[214:217], v[108:111], v[4:19]
	v_mfma_f32_32x32x16_bf16 v[84:99], v[238:241], v[104:107], v[84:99]
	v_mfma_f32_32x32x16_bf16 v[4:19], v[218:221], v[112:115], v[4:19]
	v_mfma_f32_32x32x16_bf16 v[84:99], v[222:225], v[230:233], v[84:99]
	s_nop 11
	v_add_f32_e32 v2, v99, v19
	v_mov_b32 v2, v2
	s_nop 0
	v_add_f32_e32 v2, v83, v99
	v_add_f32_e32 v82, v82, v98
	v_add_f32_e32 v81, v81, v97
	v_add_f32_e32 v80, v80, v96
	v_add_f32_e32 v79, v79, v95
	v_add_f32_e32 v78, v78, v94
	v_add_f32_e32 v77, v77, v93
	v_add_f32_e32 v76, v76, v92
	v_add_f32_e32 v75, v75, v91
	v_add_f32_e32 v74, v74, v90
	v_add_f32_e32 v73, v73, v89
	v_add_f32_e32 v72, v72, v88
	v_add_f32_e32 v71, v71, v87
	v_add_f32_e32 v70, v70, v86
	v_add_f32_e32 v69, v69, v85
	v_add_f32_e32 v68, v68, v84
	v_add_u32_e32 v83, 0x16800, v242
	ds_write2st64_b32 v83, v68, v69 offset1:1
	ds_write2st64_b32 v83, v70, v71 offset0:2 offset1:3
	ds_write2st64_b32 v83, v72, v73 offset0:8 offset1:9
	ds_write2st64_b32 v83, v74, v75 offset0:10 offset1:11
	ds_write2st64_b32 v83, v76, v77 offset0:16 offset1:17
	ds_write2st64_b32 v83, v78, v79 offset0:18 offset1:19
	ds_write2st64_b32 v83, v80, v81 offset0:24 offset1:25
	ds_write2st64_b32 v83, v82, v2 offset0:26 offset1:27
	s_mov_b64 s[4:5], 0
